# speedup vs baseline: 1.0087x; 1.0046x over previous
amdhsa.kernels:
  - .agpr_count:     0
    .args:
      - .actual_access:  read_only
        .address_space:  global
        .offset:         0
        .size:           8
        .value_kind:     global_buffer
      - .actual_access:  read_only
        .address_space:  global
        .offset:         8
        .size:           8
        .value_kind:     global_buffer
      - .actual_access:  read_only
        .address_space:  global
        .offset:         16
        .size:           8
        .value_kind:     global_buffer
      - .actual_access:  read_only
        .address_space:  global
        .offset:         24
        .size:           8
        .value_kind:     global_buffer
      - .actual_access:  read_only
        .address_space:  global
        .offset:         32
        .size:           8
        .value_kind:     global_buffer
      - .actual_access:  read_only
        .address_space:  global
        .offset:         40
        .size:           8
        .value_kind:     global_buffer
      - .actual_access:  read_only
        .address_space:  global
        .offset:         48
        .size:           8
        .value_kind:     global_buffer
      - .actual_access:  read_only
        .address_space:  global
        .offset:         56
        .size:           8
        .value_kind:     global_buffer
      - .actual_access:  read_only
        .address_space:  global
        .offset:         64
        .size:           8
        .value_kind:     global_buffer
      - .actual_access:  read_only
        .address_space:  global
        .offset:         72
        .size:           8
        .value_kind:     global_buffer
      - .actual_access:  read_only
        .address_space:  global
        .offset:         80
        .size:           8
        .value_kind:     global_buffer
      - .actual_access:  read_only
        .address_space:  global
        .offset:         88
        .size:           8
        .value_kind:     global_buffer
      - .actual_access:  read_only
        .address_space:  global
        .offset:         96
        .size:           8
        .value_kind:     global_buffer
      - .actual_access:  read_only
        .address_space:  global
        .offset:         104
        .size:           8
        .value_kind:     global_buffer
      - .actual_access:  read_only
        .address_space:  global
        .offset:         112
        .size:           8
        .value_kind:     global_buffer
      - .actual_access:  read_only
        .address_space:  global
        .offset:         120
        .size:           8
        .value_kind:     global_buffer
      - .actual_access:  write_only
        .address_space:  global
        .offset:         128
        .size:           8
        .value_kind:     global_buffer
      - .actual_access:  write_only
        .address_space:  global
        .offset:         136
        .size:           8
        .value_kind:     global_buffer
      - .actual_access:  write_only
        .address_space:  global
        .offset:         144
        .size:           8
        .value_kind:     global_buffer
    .group_segment_fixed_size: 0
    .kernarg_segment_align: 8
    .kernarg_segment_size: 152
    .language:       OpenCL C
    .language_version:
      - 2
      - 0
    .max_flat_workgroup_size: 256
    .name:           _Z11prep_kernelPKfS0_S0_S0_S0_S0_S0_S0_S0_S0_S0_S0_S0_S0_S0_S0_PtS1_S1_
    .private_segment_fixed_size: 0
    .sgpr_count:     30
    .sgpr_spill_count: 0
    .symbol:         _Z11prep_kernelPKfS0_S0_S0_S0_S0_S0_S0_S0_S0_S0_S0_S0_S0_S0_S0_PtS1_S1_.kd
    .uniform_work_group_size: 1
    .uses_dynamic_stack: false
    .vgpr_count:     8
    .vgpr_spill_count: 0
    .wavefront_size: 64
  - .agpr_count:     0
    .args:
      - .actual_access:  read_only
        .address_space:  global
        .offset:         0
        .size:           8
        .value_kind:     global_buffer
      - .actual_access:  read_only
        .address_space:  global
        .offset:         8
        .size:           8
        .value_kind:     global_buffer
      - .actual_access:  read_only
        .address_space:  global
        .offset:         16
        .size:           8
        .value_kind:     global_buffer
      - .actual_access:  read_only
        .address_space:  global
        .offset:         24
        .size:           8
        .value_kind:     global_buffer
      - .actual_access:  read_only
        .address_space:  global
        .offset:         32
        .size:           8
        .value_kind:     global_buffer
      - .actual_access:  read_only
        .address_space:  global
        .offset:         40
        .size:           8
        .value_kind:     global_buffer
      - .actual_access:  read_only
        .address_space:  global
        .offset:         48
        .size:           8
        .value_kind:     global_buffer
      - .actual_access:  read_only
        .address_space:  global
        .offset:         56
        .size:           8
        .value_kind:     global_buffer
      - .actual_access:  write_only
        .address_space:  global
        .offset:         64
        .size:           8
        .value_kind:     global_buffer
      - .actual_access:  write_only
        .address_space:  global
        .offset:         72
        .size:           8
        .value_kind:     global_buffer
      - .actual_access:  write_only
        .address_space:  global
        .offset:         80
        .size:           8
        .value_kind:     global_buffer
    .group_segment_fixed_size: 0
    .kernarg_segment_align: 8
    .kernarg_segment_size: 88
    .language:       OpenCL C
    .language_version:
      - 2
      - 0
    .max_flat_workgroup_size: 512
    .name:           _Z10rnn_kernelPKfS0_S0_S0_S0_S0_PKtS2_PfPtS3_
    .private_segment_fixed_size: 0
    .sgpr_count:     86
    .sgpr_spill_count: 0
    .symbol:         _Z10rnn_kernelPKfS0_S0_S0_S0_S0_PKtS2_PfPtS3_.kd
    .uniform_work_group_size: 1
    .uses_dynamic_stack: false
    .vgpr_count:     256
    .vgpr_spill_count: 0
    .wavefront_size: 64
  - .agpr_count:     0
    .args:
      - .actual_access:  read_only
        .address_space:  global
        .offset:         0
        .size:           8
        .value_kind:     global_buffer
      - .actual_access:  read_only
        .address_space:  global
        .offset:         8
        .size:           8
        .value_kind:     global_buffer
      - .actual_access:  read_only
        .address_space:  global
        .offset:         16
        .size:           8
        .value_kind:     global_buffer
      - .actual_access:  read_only
        .address_space:  global
        .offset:         24
        .size:           8
        .value_kind:     global_buffer
      - .actual_access:  read_only
        .address_space:  global
        .offset:         32
        .size:           8
        .value_kind:     global_buffer
      - .actual_access:  write_only
        .address_space:  global
        .offset:         40
        .size:           8
        .value_kind:     global_buffer
      - .actual_access:  write_only
        .address_space:  global
        .offset:         48
        .size:           8
        .value_kind:     global_buffer
    .group_segment_fixed_size: 0
    .kernarg_segment_align: 8
    .kernarg_segment_size: 56
    .language:       OpenCL C
    .language_version:
      - 2
      - 0
    .max_flat_workgroup_size: 1024
    .name:           _Z11attn_kernelPKtS0_PKfS2_S2_PfS3_
    .private_segment_fixed_size: 0
    .sgpr_count:     30
    .sgpr_spill_count: 0
    .symbol:         _Z11attn_kernelPKtS0_PKfS2_S2_PfS3_.kd
    .uniform_work_group_size: 1
    .uses_dynamic_stack: false
    .vgpr_count:     128
    .vgpr_spill_count: 0
    .wavefront_size: 64
  - .agpr_count:     0
    .args:
      - .actual_access:  read_only
        .address_space:  global
        .offset:         0
        .size:           8
        .value_kind:     global_buffer
      - .actual_access:  read_only
        .address_space:  global
        .offset:         8
        .size:           8
        .value_kind:     global_buffer
      - .actual_access:  read_only
        .address_space:  global
        .offset:         16
        .size:           8
        .value_kind:     global_buffer
      - .actual_access:  write_only
        .address_space:  global
        .offset:         24
        .size:           8
        .value_kind:     global_buffer
    .group_segment_fixed_size: 192
    .kernarg_segment_align: 8
    .kernarg_segment_size: 32
    .language:       OpenCL C
    .language_version:
      - 2
      - 0
    .max_flat_workgroup_size: 1024
    .name:           _Z11loss_kernelPKfS0_S0_Pf
    .private_segment_fixed_size: 0
    .sgpr_count:     14
    .sgpr_spill_count: 0
    .symbol:         _Z11loss_kernelPKfS0_S0_Pf.kd
    .uniform_work_group_size: 1
    .uses_dynamic_stack: false
    .vgpr_count:     46
    .vgpr_spill_count: 0
    .wavefront_size: 64
